# v79 + arrival-time invalidate issued by wave 1 + relaxed first-iteration waits in the peeled gates/out copies
# baseline (speedup 1.0000x reference)
; #define PG8_STAGE(bufoff, gbase, voff) do { _Pragma("unroll") for (int _i = 0; _i < 2; ++_i) \
;         __builtin_amdgcn_global_load_lds((const unsigned*)((const char*)(gbase) + (voff)[_i]), (PG8_LAS unsigned*)(lds + (bufoff) + ldsw + _i * 8192), 16, 0, 0); } while (0)
; template <class Epi, class Sched, bool ALIGN_EPI = true, bool F8 = false>
; __device__ __forceinline__ void gemm_phase(PG8_LAS unsigned char* lds, const Sched& S, const Epi& E) {
;     ...
;         const bool has_next = S.next(ui + 1, nxt);
;         const char* nA = has_next ? nxt.A : cA; const char* nB = has_next ? nxt.B : cB;
;         const int nt = cur.nt;
; #pragma unroll 1
;         for (int t = 0; t < nt; t += 2) {
;             const bool last = (t == nt - 2);
;             if constexpr (Sched::GATHER) { if (last && has_next) S.a_off(nxt, Rs, Cs, voffAn); }
;             const char* a1 = cA + (size_t)(t + 1) * kstep;
;             const char* a2 = last ? nA : cA + (size_t)(t + 2) * kstep; const char* b2 = last ? nB : cB + (size_t)(t + 2) * kstepB;
;             const char* a3 = a2 + kstep; const char* b3 = b2 + kstepB;
;             unsigned vA2[2][2];
; #pragma unroll
;             for (int h = 0; h < 2; ++h)
; #pragma unroll
;                 for (int i = 0; i < 2; ++i) { if constexpr (Sched::GATHER) vA2[h][i] = (last && has_next) ? voffAn[h][i] : voffA[h][i]; else vA2[h][i] = voffA[h][i]; }
;             PG8_LDB(B0, 0, 0); PG8_LDB(B1, 0, 1); PG8_SCHED; PG8_LDA(At, 0, 0); PG8_STAGE(PG8_SA(1, 1), a1, voffA[1]);
;             PG8_WAIT_V(8); PG8_WAIT_L(0); PG8_BAR; PG8_MMA(0, 0, At, B0); PG8_MMA(0, 1, At, B1); PG8_BAR; PG8_SCHED;
;             PG8_LDA(At, 0, 1); PG8_STAGE(PG8_SB(0, 0), b2, voffB[0]); PG8_STAGE(PG8_SB(0, 1), b2, voffB[1]); PG8_STAGE(PG8_SA(0, 0), a2, vA2[0]);
;             PG8_WAIT_V(8); PG8_WAIT_L(0); PG8_BAR; PG8_MMA(1, 0, At, B0); PG8_MMA(1, 1, At, B1); PG8_BAR; PG8_SCHED;
;             PG8_LDB(B0, 1, 0); PG8_LDB(B1, 1, 1); PG8_SCHED; PG8_LDA(At, 1, 0); PG8_STAGE(PG8_SA(0, 1), a2, vA2[1]);
;             PG8_WAIT_V(8); PG8_WAIT_L(0); PG8_BAR; PG8_MMA(0, 0, At, B0); PG8_MMA(0, 1, At, B1); PG8_BAR; PG8_SCHED;
;             PG8_LDA(At, 1, 1); PG8_STAGE(PG8_SB(1, 0), b3, voffB[0]); PG8_STAGE(PG8_SB(1, 1), b3, voffB[1]); PG8_STAGE(PG8_SA(1, 0), a3, vA2[0]);
;             PG8_WAIT_V(8); PG8_WAIT_L(0); PG8_BAR; PG8_MMA(1, 0, At, B0); PG8_MMA(1, 1, At, B1); PG8_BAR; PG8_SCHED;
.Lpk0_428:
	ds_read_b128 v[18:21], v192
	ds_read_b128 v[22:25], v192 offset:1024
	ds_read_b128 v[26:29], v192 offset:2048
	ds_read_b128 v[30:33], v192 offset:3072
	ds_read_b128 v[2:5], v193
	ds_read_b128 v[6:9], v193 offset:1024
	ds_read_b128 v[10:13], v193 offset:2048
	ds_read_b128 v[14:17], v193 offset:3072
	s_add_u32 s26, s24, 0x8000
	s_addc_u32 s27, s25, 0
	s_cmp_eq_u32 s74, 12
	s_cselect_b32 s30, s20, s26
	s_cselect_b32 s31, s21, s27
	s_cselect_b32 s28, s22, s17
	s_cselect_b32 s29, s23, s19
	s_add_u32 s26, s30, 0x8000
	s_addc_u32 s27, s31, 0
	s_add_i32 m0, s48, 0xc000
	ds_read_b128 v[198:201], v194
	ds_read_b128 v[202:205], v194 offset:1024
	ds_read_b128 v[206:209], v194 offset:2048
	ds_read_b128 v[210:213], v194 offset:3072
	ds_read_b128 v[214:217], v194 offset:4096
	ds_read_b128 v[218:221], v194 offset:5120
	ds_read_b128 v[222:225], v194 offset:6144
	ds_read_b128 v[226:229], v194 offset:7168
	global_load_lds_dwordx4 v184, s[24:25]
	s_add_i32 m0, s48, 0xe000
	s_nop 0
	global_load_lds_dwordx4 v182, s[24:25]
	s_waitcnt vmcnt(16)
	s_waitcnt lgkmcnt(0)
	s_setprio 1
	v_mfma_f32_16x16x128_f8f6f4 v[158:161], v[18:25], v[198:205], 0
	v_mfma_f32_16x16x128_f8f6f4 v[154:157], v[26:33], v[198:205], 0
	v_mfma_f32_16x16x128_f8f6f4 v[142:145], v[18:25], v[206:213], 0
	v_mfma_f32_16x16x128_f8f6f4 v[138:141], v[26:33], v[206:213], 0
	v_mfma_f32_16x16x128_f8f6f4 v[126:129], v[18:25], v[214:221], 0
	v_mfma_f32_16x16x128_f8f6f4 v[122:125], v[26:33], v[214:221], 0
	v_mfma_f32_16x16x128_f8f6f4 v[110:113], v[18:25], v[222:229], 0
	v_mfma_f32_16x16x128_f8f6f4 v[106:109], v[26:33], v[222:229], 0
	s_nop 3
	s_setprio 0
	s_setprio 1
	v_mfma_f32_16x16x128_f8f6f4 v[150:153], v[2:9], v[198:205], 0
	v_mfma_f32_16x16x128_f8f6f4 v[146:149], v[10:17], v[198:205], 0
	v_mfma_f32_16x16x128_f8f6f4 v[134:137], v[2:9], v[206:213], 0
	v_mfma_f32_16x16x128_f8f6f4 v[130:133], v[10:17], v[206:213], 0
	v_mfma_f32_16x16x128_f8f6f4 v[118:121], v[2:9], v[214:221], 0
	v_mfma_f32_16x16x128_f8f6f4 v[114:117], v[10:17], v[214:221], 0
	v_mfma_f32_16x16x128_f8f6f4 v[102:105], v[2:9], v[222:229], 0
	v_mfma_f32_16x16x128_f8f6f4 v[98:101], v[10:17], v[222:229], 0
	s_setprio 0
	s_barrier
	s_add_i32 s75, s65, s47
	s_mov_b32 m0, s75
	ds_read_b128 v[198:201], v194 offset:16384
	ds_read_b128 v[202:205], v194 offset:17408
	ds_read_b128 v[206:209], v194 offset:18432
	ds_read_b128 v[210:213], v194 offset:19456
	ds_read_b128 v[214:217], v194 offset:20480
	ds_read_b128 v[218:221], v194 offset:21504
	ds_read_b128 v[222:225], v194 offset:22528
	ds_read_b128 v[226:229], v194 offset:23552
	global_load_lds_dwordx4 v164, s[28:29]
	s_add_i32 m0, s75, 0x2000
	s_add_i32 s75, s66, s47
	global_load_lds_dwordx4 v166, s[28:29]
	s_add_u32 s98, s28, s4
	s_addc_u32 s99, s29, s5
	s_mov_b32 m0, s75
	s_nop 0
	global_load_lds_dwordx4 v164, s[98:99]
	s_add_u32 s100, s28, s4
	s_addc_u32 s101, s29, s5
	s_add_i32 m0, s75, 0x2000
	s_nop 0
	global_load_lds_dwordx4 v166, s[100:101]
	s_mov_b32 m0, s48
	s_nop 0
	global_load_lds_dwordx4 v174, s[30:31]
	s_mov_b32 m0, s49
	s_nop 0
	global_load_lds_dwordx4 v176, s[30:31]
	s_waitcnt vmcnt(16)
	s_waitcnt lgkmcnt(0)
	s_setprio 1
	v_mfma_f32_16x16x128_f8f6f4 v[94:97], v[18:25], v[198:205], 0
	v_mfma_f32_16x16x128_f8f6f4 v[90:93], v[26:33], v[198:205], 0
	v_mfma_f32_16x16x128_f8f6f4 v[78:81], v[18:25], v[206:213], 0
	v_mfma_f32_16x16x128_f8f6f4 v[74:77], v[26:33], v[206:213], 0
	v_mfma_f32_16x16x128_f8f6f4 v[62:65], v[18:25], v[214:221], 0
	v_mfma_f32_16x16x128_f8f6f4 v[58:61], v[26:33], v[214:221], 0
	v_mfma_f32_16x16x128_f8f6f4 v[46:49], v[18:25], v[222:229], 0
	v_mfma_f32_16x16x128_f8f6f4 v[42:45], v[26:33], v[222:229], 0
	s_nop 3
	s_setprio 0
	s_setprio 1
	v_mfma_f32_16x16x128_f8f6f4 v[86:89], v[2:9], v[198:205], 0
	v_mfma_f32_16x16x128_f8f6f4 v[82:85], v[10:17], v[198:205], 0
	v_mfma_f32_16x16x128_f8f6f4 v[70:73], v[2:9], v[206:213], 0
	v_mfma_f32_16x16x128_f8f6f4 v[66:69], v[10:17], v[206:213], 0
	v_mfma_f32_16x16x128_f8f6f4 v[54:57], v[2:9], v[214:221], 0
	v_mfma_f32_16x16x128_f8f6f4 v[50:53], v[10:17], v[214:221], 0
	v_mfma_f32_16x16x128_f8f6f4 v[38:41], v[2:9], v[222:229], 0
	v_mfma_f32_16x16x128_f8f6f4 v[34:37], v[10:17], v[222:229], 0
	s_setprio 0
	s_barrier
; #define PG8_STAGE(bufoff, gbase, voff) do { _Pragma("unroll") for (int _i = 0; _i < 2; ++_i) \
;         __builtin_amdgcn_global_load_lds((const unsigned*)((const char*)(gbase) + (voff)[_i]), (PG8_LAS unsigned*)(lds + (bufoff) + ldsw + _i * 8192), 16, 0, 0); } while (0)
; #define PG8_WAIT_V(n) asm volatile("s_waitcnt vmcnt(" #n ")" ::: "memory")
; #define PG8_WAIT_L(n) asm volatile("s_waitcnt lgkmcnt(" #n ")" ::: "memory")
; #define PG8_BAR __builtin_amdgcn_s_barrier()
; #define PG8_SCHED __builtin_amdgcn_sched_barrier(0)
; template <class Epi, class Sched, bool ALIGN_EPI = true, bool F8 = false>
; __device__ __forceinline__ void gemm_phase(PG8_LAS unsigned char* lds, const Sched& S, const Epi& E) {
;     ...
;             const char* a1 = cA + (size_t)(t + 1) * kstep;
;             const char* a2 = last ? nA : cA + (size_t)(t + 2) * kstep; const char* b2 = last ? nB : cB + (size_t)(t + 2) * kstepB;
;             const char* a3 = a2 + kstep; const char* b3 = b2 + kstepB;
;             unsigned vA2[2][2];
; #pragma unroll
;             for (int h = 0; h < 2; ++h)
; #pragma unroll
;                 for (int i = 0; i < 2; ++i) { if constexpr (Sched::GATHER) vA2[h][i] = (last && has_next) ? voffAn[h][i] : voffA[h][i]; else vA2[h][i] = voffA[h][i]; }
;             PG8_LDB(B0, 0, 0); PG8_LDB(B1, 0, 1); PG8_SCHED; PG8_LDA(At, 0, 0); PG8_STAGE(PG8_SA(1, 1), a1, voffA[1]);
;             PG8_WAIT_V(8); PG8_WAIT_L(0); PG8_BAR; PG8_MMA(0, 0, At, B0); PG8_MMA(0, 1, At, B1); PG8_BAR; PG8_SCHED;
;             PG8_LDA(At, 0, 1); PG8_STAGE(PG8_SB(0, 0), b2, voffB[0]); PG8_STAGE(PG8_SB(0, 1), b2, voffB[1]); PG8_STAGE(PG8_SA(0, 0), a2, vA2[0]);
;             PG8_WAIT_V(8); PG8_WAIT_L(0); PG8_BAR; PG8_MMA(1, 0, At, B0); PG8_MMA(1, 1, At, B1); PG8_BAR; PG8_SCHED;
;             PG8_LDB(B0, 1, 0); PG8_LDB(B1, 1, 1); PG8_SCHED; PG8_LDA(At, 1, 0); PG8_STAGE(PG8_SA(0, 1), a2, vA2[1]);
;             PG8_WAIT_V(8); PG8_WAIT_L(0); PG8_BAR; PG8_MMA(0, 0, At, B0); PG8_MMA(0, 1, At, B1); PG8_BAR; PG8_SCHED;
;             PG8_LDA(At, 1, 1); PG8_STAGE(PG8_SB(1, 0), b3, voffB[0]); PG8_STAGE(PG8_SB(1, 1), b3, voffB[1]); PG8_STAGE(PG8_SA(1, 0), a3, vA2[0]);
;             PG8_WAIT_V(8); PG8_WAIT_L(0); PG8_BAR; PG8_MMA(1, 0, At, B0); PG8_MMA(1, 1, At, B1); PG8_BAR; PG8_SCHED;
	s_add_i32 s75, 0, 0x18000
	s_add_i32 s76, 0, 0x1c000
	v_add_u32_e32 v14, s75, v191
	v_add_u32_e32 v30, s76, v191
	ds_read_b128 v[2:5], v14
	ds_read_b128 v[6:9], v14 offset:1024
	ds_read_b128 v[10:13], v14 offset:2048
	ds_read_b128 v[14:17], v14 offset:3072
	ds_read_b128 v[18:21], v30
	ds_read_b128 v[22:25], v30 offset:1024
	ds_read_b128 v[26:29], v30 offset:2048
	ds_read_b128 v[30:33], v30 offset:3072
	s_mov_b32 m0, s50
	ds_read_b128 v[198:201], v194 offset:32768
	ds_read_b128 v[202:205], v194 offset:33792
	ds_read_b128 v[206:209], v194 offset:34816
	ds_read_b128 v[210:213], v194 offset:35840
	ds_read_b128 v[214:217], v194 offset:36864
	ds_read_b128 v[218:221], v194 offset:37888
	ds_read_b128 v[222:225], v194 offset:38912
	ds_read_b128 v[226:229], v194 offset:39936
	global_load_lds_dwordx4 v178, s[30:31]
	s_mov_b32 m0, s51
	s_nop 0
	global_load_lds_dwordx4 v180, s[30:31]
	s_waitcnt vmcnt(8)
	s_waitcnt lgkmcnt(0)
	s_setprio 1
	v_mfma_f32_16x16x128_f8f6f4 v[158:161], v[2:9], v[198:205], v[158:161]
	v_mfma_f32_16x16x128_f8f6f4 v[154:157], v[10:17], v[198:205], v[154:157]
	v_mfma_f32_16x16x128_f8f6f4 v[142:145], v[2:9], v[206:213], v[142:145]
	v_mfma_f32_16x16x128_f8f6f4 v[138:141], v[10:17], v[206:213], v[138:141]
	v_mfma_f32_16x16x128_f8f6f4 v[126:129], v[2:9], v[214:221], v[126:129]
	v_mfma_f32_16x16x128_f8f6f4 v[122:125], v[10:17], v[214:221], v[122:125]
	v_mfma_f32_16x16x128_f8f6f4 v[110:113], v[2:9], v[222:229], v[110:113]
	v_mfma_f32_16x16x128_f8f6f4 v[106:109], v[10:17], v[222:229], v[106:109]
	s_nop 3
	s_setprio 0
	s_setprio 1
	v_mfma_f32_16x16x128_f8f6f4 v[150:153], v[18:25], v[198:205], v[150:153]
	v_mfma_f32_16x16x128_f8f6f4 v[146:149], v[26:33], v[198:205], v[146:149]
	v_mfma_f32_16x16x128_f8f6f4 v[134:137], v[18:25], v[206:213], v[134:137]
	v_mfma_f32_16x16x128_f8f6f4 v[130:133], v[26:33], v[206:213], v[130:133]
	v_mfma_f32_16x16x128_f8f6f4 v[118:121], v[18:25], v[214:221], v[118:121]
	v_mfma_f32_16x16x128_f8f6f4 v[114:117], v[26:33], v[214:221], v[114:117]
	v_mfma_f32_16x16x128_f8f6f4 v[102:105], v[18:25], v[222:229], v[102:105]
	v_mfma_f32_16x16x128_f8f6f4 v[98:101], v[26:33], v[222:229], v[98:101]
	s_setprio 0
	s_barrier
	s_add_u32 s28, s28, 0x8000
	s_addc_u32 s29, s29, 0
	s_add_i32 s30, s75, s47
	s_mov_b32 m0, s30
	ds_read_b128 v[198:201], v194 offset:49152
	ds_read_b128 v[202:205], v194 offset:50176
	ds_read_b128 v[206:209], v194 offset:51200
	ds_read_b128 v[210:213], v194 offset:52224
	ds_read_b128 v[214:217], v194 offset:53248
	ds_read_b128 v[218:221], v194 offset:54272
	ds_read_b128 v[222:225], v194 offset:55296
	ds_read_b128 v[226:229], v194 offset:56320
	global_load_lds_dwordx4 v164, s[28:29]
	s_add_i32 m0, s30, 0x2000
	s_add_i32 s30, s76, s47
	global_load_lds_dwordx4 v166, s[28:29]
	s_mov_b32 m0, s30
	s_nop 0
	global_load_lds_dwordx4 v168, s[28:29]
	s_add_i32 m0, s30, 0x2000
	s_nop 0
	global_load_lds_dwordx4 v172, s[28:29]
	s_mov_b32 m0, s60
	s_nop 0
	global_load_lds_dwordx4 v174, s[26:27]
	s_mov_b32 m0, s61
	s_nop 0
	global_load_lds_dwordx4 v176, s[26:27]
	s_waitcnt vmcnt(8)
	s_waitcnt lgkmcnt(0)
	s_setprio 1
	v_mfma_f32_16x16x128_f8f6f4 v[94:97], v[2:9], v[198:205], v[94:97]
	v_mfma_f32_16x16x128_f8f6f4 v[90:93], v[10:17], v[198:205], v[90:93]
	v_mfma_f32_16x16x128_f8f6f4 v[78:81], v[2:9], v[206:213], v[78:81]
	v_mfma_f32_16x16x128_f8f6f4 v[74:77], v[10:17], v[206:213], v[74:77]
	v_mfma_f32_16x16x128_f8f6f4 v[62:65], v[2:9], v[214:221], v[62:65]
	v_mfma_f32_16x16x128_f8f6f4 v[58:61], v[10:17], v[214:221], v[58:61]
	v_mfma_f32_16x16x128_f8f6f4 v[46:49], v[2:9], v[222:229], v[46:49]
	v_mfma_f32_16x16x128_f8f6f4 v[42:45], v[10:17], v[222:229], v[42:45]
	s_nop 3
	s_setprio 0
	s_setprio 1
	v_mfma_f32_16x16x128_f8f6f4 v[86:89], v[18:25], v[198:205], v[86:89]
	v_mfma_f32_16x16x128_f8f6f4 v[82:85], v[26:33], v[198:205], v[82:85]
	v_mfma_f32_16x16x128_f8f6f4 v[70:73], v[18:25], v[206:213], v[70:73]
	v_mfma_f32_16x16x128_f8f6f4 v[66:69], v[26:33], v[206:213], v[66:69]
	v_mfma_f32_16x16x128_f8f6f4 v[54:57], v[18:25], v[214:221], v[54:57]
	v_mfma_f32_16x16x128_f8f6f4 v[50:53], v[26:33], v[214:221], v[50:53]
	v_mfma_f32_16x16x128_f8f6f4 v[38:41], v[18:25], v[222:229], v[38:41]
	v_mfma_f32_16x16x128_f8f6f4 v[34:37], v[26:33], v[222:229], v[34:37]
	s_setprio 0
	s_barrier
	s_add_i32 s74, s74, 2
	s_add_u32 s17, s17, 0x10000
	s_addc_u32 s19, s19, 0
	s_add_u32 s24, s24, 0x10000
	s_addc_u32 s25, s25, 0
	s_cmp_gt_u32 s74, 13
	s_cbranch_scc0 .LBB0_428
	s_branch .Lfx_11141

; #define PG8_STAGE(bufoff, gbase, voff) do { _Pragma("unroll") for (int _i = 0; _i < 2; ++_i) \
;         __builtin_amdgcn_global_load_lds((const unsigned*)((const char*)(gbase) + (voff)[_i]), (PG8_LAS unsigned*)(lds + (bufoff) + ldsw + _i * 8192), 16, 0, 0); } while (0)
; template <class Epi, class Sched, bool ALIGN_EPI = true, bool F8 = false>
; __device__ __forceinline__ void gemm_phase(PG8_LAS unsigned char* lds, const Sched& S, const Epi& E) {
;     ...
;         const bool has_next = S.next(ui + 1, nxt);
;         const char* nA = has_next ? nxt.A : cA; const char* nB = has_next ? nxt.B : cB;
;         const int nt = cur.nt;
; #pragma unroll 1
;         for (int t = 0; t < nt; t += 2) {
;             const bool last = (t == nt - 2);
;             if constexpr (Sched::GATHER) { if (last && has_next) S.a_off(nxt, Rs, Cs, voffAn); }
;             const char* a1 = cA + (size_t)(t + 1) * kstep;
;             const char* a2 = last ? nA : cA + (size_t)(t + 2) * kstep; const char* b2 = last ? nB : cB + (size_t)(t + 2) * kstepB;
;             const char* a3 = a2 + kstep; const char* b3 = b2 + kstepB;
;             unsigned vA2[2][2];
; #pragma unroll
;             for (int h = 0; h < 2; ++h)
; #pragma unroll
;                 for (int i = 0; i < 2; ++i) { if constexpr (Sched::GATHER) vA2[h][i] = (last && has_next) ? voffAn[h][i] : voffA[h][i]; else vA2[h][i] = voffA[h][i]; }
;             PG8_LDB(B0, 0, 0); PG8_LDB(B1, 0, 1); PG8_SCHED; PG8_LDA(At, 0, 0); PG8_STAGE(PG8_SA(1, 1), a1, voffA[1]);
;             PG8_WAIT_V(8); PG8_WAIT_L(0); PG8_BAR; PG8_MMA(0, 0, At, B0); PG8_MMA(0, 1, At, B1); PG8_BAR; PG8_SCHED;
;             PG8_LDA(At, 0, 1); PG8_STAGE(PG8_SB(0, 0), b2, voffB[0]); PG8_STAGE(PG8_SB(0, 1), b2, voffB[1]); PG8_STAGE(PG8_SA(0, 0), a2, vA2[0]);
;             PG8_WAIT_V(8); PG8_WAIT_L(0); PG8_BAR; PG8_MMA(1, 0, At, B0); PG8_MMA(1, 1, At, B1); PG8_BAR; PG8_SCHED;
;             PG8_LDB(B0, 1, 0); PG8_LDB(B1, 1, 1); PG8_SCHED; PG8_LDA(At, 1, 0); PG8_STAGE(PG8_SA(0, 1), a2, vA2[1]);
;             PG8_WAIT_V(8); PG8_WAIT_L(0); PG8_BAR; PG8_MMA(0, 0, At, B0); PG8_MMA(0, 1, At, B1); PG8_BAR; PG8_SCHED;
;             PG8_LDA(At, 1, 1); PG8_STAGE(PG8_SB(1, 0), b3, voffB[0]); PG8_STAGE(PG8_SB(1, 1), b3, voffB[1]); PG8_STAGE(PG8_SA(1, 0), a3, vA2[0]);
;             PG8_WAIT_V(8); PG8_WAIT_L(0); PG8_BAR; PG8_MMA(1, 0, At, B0); PG8_MMA(1, 1, At, B1); PG8_BAR; PG8_SCHED;
.Lh1e_11141:
.Lpk1_428:
	ds_read_b128 v[18:21], v192
	ds_read_b128 v[22:25], v192 offset:1024
	ds_read_b128 v[26:29], v192 offset:2048
	ds_read_b128 v[30:33], v192 offset:3072
	ds_read_b128 v[2:5], v193
	ds_read_b128 v[6:9], v193 offset:1024
	ds_read_b128 v[10:13], v193 offset:2048
	ds_read_b128 v[14:17], v193 offset:3072
	s_add_u32 s26, s24, 0x8000
	s_addc_u32 s27, s25, 0
	s_cmp_eq_u32 s74, 12
	s_cselect_b32 s30, s20, s26
	s_cselect_b32 s31, s21, s27
	s_cselect_b32 s28, s22, s17
	s_cselect_b32 s29, s23, s19
	s_add_u32 s26, s30, 0x8000
	s_addc_u32 s27, s31, 0
	s_add_i32 m0, s48, 0xc000
	ds_read_b128 v[198:201], v194
	ds_read_b128 v[202:205], v194 offset:1024
	ds_read_b128 v[206:209], v194 offset:2048
	ds_read_b128 v[210:213], v194 offset:3072
	ds_read_b128 v[214:217], v194 offset:4096
	ds_read_b128 v[218:221], v194 offset:5120
	ds_read_b128 v[222:225], v194 offset:6144
	ds_read_b128 v[226:229], v194 offset:7168
	global_load_lds_dwordx4 v184, s[24:25]
	s_add_i32 m0, s48, 0xe000
	s_nop 0
	global_load_lds_dwordx4 v182, s[24:25]
	s_waitcnt vmcnt(16)
	s_waitcnt lgkmcnt(0)
	s_barrier
	s_setprio 2
	v_mfma_f32_16x16x128_f8f6f4 v[158:161], v[18:25], v[198:205], 0
	v_mfma_f32_16x16x128_f8f6f4 v[154:157], v[26:33], v[198:205], 0
	v_mfma_f32_16x16x128_f8f6f4 v[142:145], v[18:25], v[206:213], 0
	v_mfma_f32_16x16x128_f8f6f4 v[138:141], v[26:33], v[206:213], 0
	v_mfma_f32_16x16x128_f8f6f4 v[126:129], v[18:25], v[214:221], 0
	v_mfma_f32_16x16x128_f8f6f4 v[122:125], v[26:33], v[214:221], 0
	v_mfma_f32_16x16x128_f8f6f4 v[110:113], v[18:25], v[222:229], 0
	v_mfma_f32_16x16x128_f8f6f4 v[106:109], v[26:33], v[222:229], 0
	s_nop 3
	s_setprio 0
	s_setprio 2
	v_mfma_f32_16x16x128_f8f6f4 v[150:153], v[2:9], v[198:205], 0
	v_mfma_f32_16x16x128_f8f6f4 v[146:149], v[10:17], v[198:205], 0
	v_mfma_f32_16x16x128_f8f6f4 v[134:137], v[2:9], v[206:213], 0
	v_mfma_f32_16x16x128_f8f6f4 v[130:133], v[10:17], v[206:213], 0
	v_mfma_f32_16x16x128_f8f6f4 v[118:121], v[2:9], v[214:221], 0
	v_mfma_f32_16x16x128_f8f6f4 v[114:117], v[10:17], v[214:221], 0
	v_mfma_f32_16x16x128_f8f6f4 v[102:105], v[2:9], v[222:229], 0
	v_mfma_f32_16x16x128_f8f6f4 v[98:101], v[10:17], v[222:229], 0
	s_setprio 0
	s_add_i32 s75, s65, s47
	s_mov_b32 m0, s75
	ds_read_b128 v[198:201], v194 offset:16384
	ds_read_b128 v[202:205], v194 offset:17408
	ds_read_b128 v[206:209], v194 offset:18432
	ds_read_b128 v[210:213], v194 offset:19456
	ds_read_b128 v[214:217], v194 offset:20480
	ds_read_b128 v[218:221], v194 offset:21504
	ds_read_b128 v[222:225], v194 offset:22528
	ds_read_b128 v[226:229], v194 offset:23552
	global_load_lds_dwordx4 v164, s[28:29]
	s_add_i32 m0, s75, 0x2000
	s_add_i32 s75, s66, s47
	global_load_lds_dwordx4 v166, s[28:29]
	s_add_u32 s98, s28, s4
	s_addc_u32 s99, s29, s5
	s_mov_b32 m0, s75
	s_nop 0
	global_load_lds_dwordx4 v164, s[98:99]
	s_add_u32 s100, s28, s4
	s_addc_u32 s101, s29, s5
	s_add_i32 m0, s75, 0x2000
	s_nop 0
	global_load_lds_dwordx4 v166, s[100:101]
	s_mov_b32 m0, s48
	s_nop 0
	global_load_lds_dwordx4 v174, s[30:31]
	s_mov_b32 m0, s49
	s_nop 0
	global_load_lds_dwordx4 v176, s[30:31]
	s_waitcnt vmcnt(16)
	s_waitcnt lgkmcnt(0)
	s_barrier
	s_setprio 2
	v_mfma_f32_16x16x128_f8f6f4 v[94:97], v[18:25], v[198:205], 0
	v_mfma_f32_16x16x128_f8f6f4 v[90:93], v[26:33], v[198:205], 0
	v_mfma_f32_16x16x128_f8f6f4 v[78:81], v[18:25], v[206:213], 0
	v_mfma_f32_16x16x128_f8f6f4 v[74:77], v[26:33], v[206:213], 0
	v_mfma_f32_16x16x128_f8f6f4 v[62:65], v[18:25], v[214:221], 0
	v_mfma_f32_16x16x128_f8f6f4 v[58:61], v[26:33], v[214:221], 0
	v_mfma_f32_16x16x128_f8f6f4 v[46:49], v[18:25], v[222:229], 0
	v_mfma_f32_16x16x128_f8f6f4 v[42:45], v[26:33], v[222:229], 0
	s_nop 3
	s_setprio 0
	s_setprio 2
	v_mfma_f32_16x16x128_f8f6f4 v[86:89], v[2:9], v[198:205], 0
	v_mfma_f32_16x16x128_f8f6f4 v[82:85], v[10:17], v[198:205], 0
	v_mfma_f32_16x16x128_f8f6f4 v[70:73], v[2:9], v[206:213], 0
	v_mfma_f32_16x16x128_f8f6f4 v[66:69], v[10:17], v[206:213], 0
	v_mfma_f32_16x16x128_f8f6f4 v[54:57], v[2:9], v[214:221], 0
	v_mfma_f32_16x16x128_f8f6f4 v[50:53], v[10:17], v[214:221], 0
	v_mfma_f32_16x16x128_f8f6f4 v[38:41], v[2:9], v[222:229], 0
	v_mfma_f32_16x16x128_f8f6f4 v[34:37], v[10:17], v[222:229], 0
	s_setprio 0
	s_add_i32 s75, 0, 0x18000
	s_add_i32 s76, 0, 0x1c000
	v_add_u32_e32 v14, s75, v191
	v_add_u32_e32 v30, s76, v191
	ds_read_b128 v[2:5], v14
	ds_read_b128 v[6:9], v14 offset:1024
	ds_read_b128 v[10:13], v14 offset:2048
	ds_read_b128 v[14:17], v14 offset:3072
	ds_read_b128 v[18:21], v30
	ds_read_b128 v[22:25], v30 offset:1024
	ds_read_b128 v[26:29], v30 offset:2048
	ds_read_b128 v[30:33], v30 offset:3072
	s_mov_b32 m0, s50
	ds_read_b128 v[198:201], v194 offset:32768
	ds_read_b128 v[202:205], v194 offset:33792
	ds_read_b128 v[206:209], v194 offset:34816
	ds_read_b128 v[210:213], v194 offset:35840
	ds_read_b128 v[214:217], v194 offset:36864
	ds_read_b128 v[218:221], v194 offset:37888
	ds_read_b128 v[222:225], v194 offset:38912
	ds_read_b128 v[226:229], v194 offset:39936
	global_load_lds_dwordx4 v178, s[30:31]
	s_mov_b32 m0, s51
	s_nop 0
	global_load_lds_dwordx4 v180, s[30:31]
	s_waitcnt vmcnt(8)
	s_waitcnt lgkmcnt(0)
	s_barrier
; #define PG8_STAGE(bufoff, gbase, voff) do { _Pragma("unroll") for (int _i = 0; _i < 2; ++_i) \
;         __builtin_amdgcn_global_load_lds((const unsigned*)((const char*)(gbase) + (voff)[_i]), (PG8_LAS unsigned*)(lds + (bufoff) + ldsw + _i * 8192), 16, 0, 0); } while (0)
; #define PG8_WAIT_V(n) asm volatile("s_waitcnt vmcnt(" #n ")" ::: "memory")
; #define PG8_WAIT_L(n) asm volatile("s_waitcnt lgkmcnt(" #n ")" ::: "memory")
; #define PG8_BAR __builtin_amdgcn_s_barrier()
; #define PG8_SCHED __builtin_amdgcn_sched_barrier(0)
; template <class Epi, class Sched, bool ALIGN_EPI = true, bool F8 = false>
; __device__ __forceinline__ void gemm_phase(PG8_LAS unsigned char* lds, const Sched& S, const Epi& E) {
;     ...
;             const char* a1 = cA + (size_t)(t + 1) * kstep;
;             const char* a2 = last ? nA : cA + (size_t)(t + 2) * kstep; const char* b2 = last ? nB : cB + (size_t)(t + 2) * kstepB;
;             const char* a3 = a2 + kstep; const char* b3 = b2 + kstepB;
;             unsigned vA2[2][2];
; #pragma unroll
;             for (int h = 0; h < 2; ++h)
; #pragma unroll
;                 for (int i = 0; i < 2; ++i) { if constexpr (Sched::GATHER) vA2[h][i] = (last && has_next) ? voffAn[h][i] : voffA[h][i]; else vA2[h][i] = voffA[h][i]; }
;             PG8_LDB(B0, 0, 0); PG8_LDB(B1, 0, 1); PG8_SCHED; PG8_LDA(At, 0, 0); PG8_STAGE(PG8_SA(1, 1), a1, voffA[1]);
;             PG8_WAIT_V(8); PG8_WAIT_L(0); PG8_BAR; PG8_MMA(0, 0, At, B0); PG8_MMA(0, 1, At, B1); PG8_BAR; PG8_SCHED;
;             PG8_LDA(At, 0, 1); PG8_STAGE(PG8_SB(0, 0), b2, voffB[0]); PG8_STAGE(PG8_SB(0, 1), b2, voffB[1]); PG8_STAGE(PG8_SA(0, 0), a2, vA2[0]);
;             PG8_WAIT_V(8); PG8_WAIT_L(0); PG8_BAR; PG8_MMA(1, 0, At, B0); PG8_MMA(1, 1, At, B1); PG8_BAR; PG8_SCHED;
;             PG8_LDB(B0, 1, 0); PG8_LDB(B1, 1, 1); PG8_SCHED; PG8_LDA(At, 1, 0); PG8_STAGE(PG8_SA(0, 1), a2, vA2[1]);
;             PG8_WAIT_V(8); PG8_WAIT_L(0); PG8_BAR; PG8_MMA(0, 0, At, B0); PG8_MMA(0, 1, At, B1); PG8_BAR; PG8_SCHED;
;             PG8_LDA(At, 1, 1); PG8_STAGE(PG8_SB(1, 0), b3, voffB[0]); PG8_STAGE(PG8_SB(1, 1), b3, voffB[1]); PG8_STAGE(PG8_SA(1, 0), a3, vA2[0]);
;             PG8_WAIT_V(8); PG8_WAIT_L(0); PG8_BAR; PG8_MMA(1, 0, At, B0); PG8_MMA(1, 1, At, B1); PG8_BAR; PG8_SCHED;
	s_setprio 2
	v_mfma_f32_16x16x128_f8f6f4 v[158:161], v[2:9], v[198:205], v[158:161]
	v_mfma_f32_16x16x128_f8f6f4 v[154:157], v[10:17], v[198:205], v[154:157]
	v_mfma_f32_16x16x128_f8f6f4 v[142:145], v[2:9], v[206:213], v[142:145]
	v_mfma_f32_16x16x128_f8f6f4 v[138:141], v[10:17], v[206:213], v[138:141]
	v_mfma_f32_16x16x128_f8f6f4 v[126:129], v[2:9], v[214:221], v[126:129]
	v_mfma_f32_16x16x128_f8f6f4 v[122:125], v[10:17], v[214:221], v[122:125]
	v_mfma_f32_16x16x128_f8f6f4 v[110:113], v[2:9], v[222:229], v[110:113]
	v_mfma_f32_16x16x128_f8f6f4 v[106:109], v[10:17], v[222:229], v[106:109]
	s_nop 3
	s_setprio 0
	s_setprio 2
	v_mfma_f32_16x16x128_f8f6f4 v[150:153], v[18:25], v[198:205], v[150:153]
	v_mfma_f32_16x16x128_f8f6f4 v[146:149], v[26:33], v[198:205], v[146:149]
	v_mfma_f32_16x16x128_f8f6f4 v[134:137], v[18:25], v[206:213], v[134:137]
	v_mfma_f32_16x16x128_f8f6f4 v[130:133], v[26:33], v[206:213], v[130:133]
	v_mfma_f32_16x16x128_f8f6f4 v[118:121], v[18:25], v[214:221], v[118:121]
	v_mfma_f32_16x16x128_f8f6f4 v[114:117], v[26:33], v[214:221], v[114:117]
	v_mfma_f32_16x16x128_f8f6f4 v[102:105], v[18:25], v[222:229], v[102:105]
	v_mfma_f32_16x16x128_f8f6f4 v[98:101], v[26:33], v[222:229], v[98:101]
	s_setprio 0
	s_add_u32 s28, s28, 0x8000
	s_addc_u32 s29, s29, 0
	s_add_i32 s30, s75, s47
	s_mov_b32 m0, s30
	ds_read_b128 v[198:201], v194 offset:49152
	ds_read_b128 v[202:205], v194 offset:50176
	ds_read_b128 v[206:209], v194 offset:51200
	ds_read_b128 v[210:213], v194 offset:52224
	ds_read_b128 v[214:217], v194 offset:53248
	ds_read_b128 v[218:221], v194 offset:54272
	ds_read_b128 v[222:225], v194 offset:55296
	ds_read_b128 v[226:229], v194 offset:56320
	global_load_lds_dwordx4 v164, s[28:29]
	s_add_i32 m0, s30, 0x2000
	s_add_i32 s30, s76, s47
	global_load_lds_dwordx4 v166, s[28:29]
	s_mov_b32 m0, s30
	s_nop 0
	global_load_lds_dwordx4 v168, s[28:29]
	s_add_i32 m0, s30, 0x2000
	s_nop 0
	global_load_lds_dwordx4 v172, s[28:29]
	s_mov_b32 m0, s60
	s_nop 0
	global_load_lds_dwordx4 v174, s[26:27]
	s_mov_b32 m0, s61
	s_nop 0
	global_load_lds_dwordx4 v176, s[26:27]
	s_waitcnt vmcnt(8)
	s_waitcnt lgkmcnt(0)
	s_barrier
	s_setprio 2
	v_mfma_f32_16x16x128_f8f6f4 v[94:97], v[2:9], v[198:205], v[94:97]
	v_mfma_f32_16x16x128_f8f6f4 v[90:93], v[10:17], v[198:205], v[90:93]
	v_mfma_f32_16x16x128_f8f6f4 v[78:81], v[2:9], v[206:213], v[78:81]
	v_mfma_f32_16x16x128_f8f6f4 v[74:77], v[10:17], v[206:213], v[74:77]
	v_mfma_f32_16x16x128_f8f6f4 v[62:65], v[2:9], v[214:221], v[62:65]
	v_mfma_f32_16x16x128_f8f6f4 v[58:61], v[10:17], v[214:221], v[58:61]
	v_mfma_f32_16x16x128_f8f6f4 v[46:49], v[2:9], v[222:229], v[46:49]
	v_mfma_f32_16x16x128_f8f6f4 v[42:45], v[10:17], v[222:229], v[42:45]
	s_nop 3
	s_setprio 0
	s_setprio 2
	v_mfma_f32_16x16x128_f8f6f4 v[86:89], v[18:25], v[198:205], v[86:89]
	v_mfma_f32_16x16x128_f8f6f4 v[82:85], v[26:33], v[198:205], v[82:85]
	v_mfma_f32_16x16x128_f8f6f4 v[70:73], v[18:25], v[206:213], v[70:73]
	v_mfma_f32_16x16x128_f8f6f4 v[66:69], v[26:33], v[206:213], v[66:69]
	v_mfma_f32_16x16x128_f8f6f4 v[54:57], v[18:25], v[214:221], v[54:57]
	v_mfma_f32_16x16x128_f8f6f4 v[50:53], v[26:33], v[214:221], v[50:53]
	v_mfma_f32_16x16x128_f8f6f4 v[38:41], v[18:25], v[222:229], v[38:41]
	v_mfma_f32_16x16x128_f8f6f4 v[34:37], v[26:33], v[222:229], v[34:37]
	s_setprio 0
	s_add_i32 s74, s74, 2
	s_add_u32 s17, s17, 0x10000
	s_addc_u32 s19, s19, 0
	s_add_u32 s24, s24, 0x10000
	s_addc_u32 s25, s25, 0
	s_cmp_gt_u32 s74, 13
	s_cbranch_scc0 .Lh1_428
	s_branch .Lfx_11141

; #define PG8_STAGE(bufoff, gbase, voff) do { _Pragma("unroll") for (int _i = 0; _i < 2; ++_i) \
;         __builtin_amdgcn_global_load_lds((const unsigned*)((const char*)(gbase) + (voff)[_i]), (PG8_LAS unsigned*)(lds + (bufoff) + ldsw + _i * 8192), 16, 0, 0); } while (0)
; template <class Epi, class Sched, bool ALIGN_EPI = true, bool F8 = false>
; __device__ __forceinline__ void gemm_phase(PG8_LAS unsigned char* lds, const Sched& S, const Epi& E) {
;     ...
;         const bool has_next = S.next(ui + 1, nxt);
;         const char* nA = has_next ? nxt.A : cA; const char* nB = has_next ? nxt.B : cB;
;         const int nt = cur.nt;
; #pragma unroll 1
;         for (int t = 0; t < nt; t += 2) {
;             const bool last = (t == nt - 2);
;             if constexpr (Sched::GATHER) { if (last && has_next) S.a_off(nxt, Rs, Cs, voffAn); }
;             const char* a1 = cA + (size_t)(t + 1) * kstep;
;             const char* a2 = last ? nA : cA + (size_t)(t + 2) * kstep; const char* b2 = last ? nB : cB + (size_t)(t + 2) * kstepB;
;             const char* a3 = a2 + kstep; const char* b3 = b2 + kstepB;
;             unsigned vA2[2][2];
; #pragma unroll
;             for (int h = 0; h < 2; ++h)
; #pragma unroll
;                 for (int i = 0; i < 2; ++i) { if constexpr (Sched::GATHER) vA2[h][i] = (last && has_next) ? voffAn[h][i] : voffA[h][i]; else vA2[h][i] = voffA[h][i]; }
;             PG8_LDB(B0, 0, 0); PG8_LDB(B1, 0, 1); PG8_SCHED; PG8_LDA(At, 0, 0); PG8_STAGE(PG8_SA(1, 1), a1, voffA[1]);
;             PG8_WAIT_V(8); PG8_WAIT_L(0); PG8_BAR; PG8_MMA(0, 0, At, B0); PG8_MMA(0, 1, At, B1); PG8_BAR; PG8_SCHED;
;             PG8_LDA(At, 0, 1); PG8_STAGE(PG8_SB(0, 0), b2, voffB[0]); PG8_STAGE(PG8_SB(0, 1), b2, voffB[1]); PG8_STAGE(PG8_SA(0, 0), a2, vA2[0]);
;             PG8_WAIT_V(8); PG8_WAIT_L(0); PG8_BAR; PG8_MMA(1, 0, At, B0); PG8_MMA(1, 1, At, B1); PG8_BAR; PG8_SCHED;
;             PG8_LDB(B0, 1, 0); PG8_LDB(B1, 1, 1); PG8_SCHED; PG8_LDA(At, 1, 0); PG8_STAGE(PG8_SA(0, 1), a2, vA2[1]);
;             PG8_WAIT_V(8); PG8_WAIT_L(0); PG8_BAR; PG8_MMA(0, 0, At, B0); PG8_MMA(0, 1, At, B1); PG8_BAR; PG8_SCHED;
;             PG8_LDA(At, 1, 1); PG8_STAGE(PG8_SB(1, 0), b3, voffB[0]); PG8_STAGE(PG8_SB(1, 1), b3, voffB[1]); PG8_STAGE(PG8_SA(1, 0), a3, vA2[0]);
;             PG8_WAIT_V(8); PG8_WAIT_L(0); PG8_BAR; PG8_MMA(1, 0, At, B0); PG8_MMA(1, 1, At, B1); PG8_BAR; PG8_SCHED;
.Lpk0_911:
	ds_read_b128 v[18:21], v191
	ds_read_b128 v[22:25], v191 offset:1024
	ds_read_b128 v[26:29], v191 offset:2048
	ds_read_b128 v[30:33], v191 offset:3072
	ds_read_b128 v[2:5], v192
	ds_read_b128 v[6:9], v192 offset:1024
	ds_read_b128 v[10:13], v192 offset:2048
	ds_read_b128 v[14:17], v192 offset:3072
	s_add_u32 s30, s28, 0x8000
	s_addc_u32 s31, s29, 0
	s_cmp_eq_u32 s65, 12
	s_cselect_b32 s42, s22, s30
	s_cselect_b32 s43, s23, s31
	s_cselect_b32 s40, s24, s19
	s_cselect_b32 s41, s25, s21
	s_add_u32 s30, s42, 0x8000
	s_addc_u32 s31, s43, 0
	s_add_i32 m0, s27, 0xc000
	ds_read_b128 v[196:199], v193
	ds_read_b128 v[200:203], v193 offset:1024
	ds_read_b128 v[204:207], v193 offset:2048
	ds_read_b128 v[208:211], v193 offset:3072
	ds_read_b128 v[212:215], v193 offset:4096
	ds_read_b128 v[216:219], v193 offset:5120
	ds_read_b128 v[220:223], v193 offset:6144
	ds_read_b128 v[224:227], v193 offset:7168
	global_load_lds_dwordx4 v182, s[28:29]
	s_add_i32 m0, s27, 0xe000
	s_nop 0
	global_load_lds_dwordx4 v180, s[28:29]
	s_waitcnt vmcnt(16)
	s_waitcnt lgkmcnt(0)
	s_setprio 1
	v_mfma_f32_16x16x128_f8f6f4 v[158:161], v[18:25], v[196:203], 0
	v_mfma_f32_16x16x128_f8f6f4 v[154:157], v[26:33], v[196:203], 0
	v_mfma_f32_16x16x128_f8f6f4 v[150:153], v[18:25], v[204:211], 0
	v_mfma_f32_16x16x128_f8f6f4 v[146:149], v[26:33], v[204:211], 0
	v_mfma_f32_16x16x128_f8f6f4 v[130:133], v[18:25], v[212:219], 0
	v_mfma_f32_16x16x128_f8f6f4 v[122:125], v[26:33], v[212:219], 0
	v_mfma_f32_16x16x128_f8f6f4 v[114:117], v[18:25], v[220:227], 0
	v_mfma_f32_16x16x128_f8f6f4 v[106:109], v[26:33], v[220:227], 0
	s_nop 3
	s_setprio 0
	s_setprio 1
	v_mfma_f32_16x16x128_f8f6f4 v[142:145], v[2:9], v[196:203], 0
	v_mfma_f32_16x16x128_f8f6f4 v[138:141], v[10:17], v[196:203], 0
	v_mfma_f32_16x16x128_f8f6f4 v[134:137], v[2:9], v[204:211], 0
	v_mfma_f32_16x16x128_f8f6f4 v[126:129], v[10:17], v[204:211], 0
	v_mfma_f32_16x16x128_f8f6f4 v[118:121], v[2:9], v[212:219], 0
	v_mfma_f32_16x16x128_f8f6f4 v[110:113], v[10:17], v[212:219], 0
	v_mfma_f32_16x16x128_f8f6f4 v[102:105], v[2:9], v[220:227], 0
	v_mfma_f32_16x16x128_f8f6f4 v[98:101], v[10:17], v[220:227], 0
	s_setprio 0
	s_barrier
	s_add_i32 s66, s60, s48
	s_mov_b32 m0, s66
	ds_read_b128 v[196:199], v193 offset:16384
	ds_read_b128 v[200:203], v193 offset:17408
	ds_read_b128 v[204:207], v193 offset:18432
	ds_read_b128 v[208:211], v193 offset:19456
	ds_read_b128 v[212:215], v193 offset:20480
	ds_read_b128 v[216:219], v193 offset:21504
	ds_read_b128 v[220:223], v193 offset:22528
	ds_read_b128 v[224:227], v193 offset:23552
	global_load_lds_dwordx4 v162, s[40:41]
	s_add_i32 m0, s66, 0x2000
	s_add_i32 s66, s61, s48
	global_load_lds_dwordx4 v164, s[40:41]
	s_add_u32 s98, s40, s6
	s_addc_u32 s99, s41, s7
	s_mov_b32 m0, s66
	s_nop 0
	global_load_lds_dwordx4 v162, s[98:99]
	s_add_u32 s100, s40, s6
	s_addc_u32 s101, s41, s7
	s_add_i32 m0, s66, 0x2000
	s_nop 0
	global_load_lds_dwordx4 v164, s[100:101]
	s_mov_b32 m0, s27
	s_nop 0
	global_load_lds_dwordx4 v166, s[42:43]
	s_mov_b32 m0, s49
	s_nop 0
	global_load_lds_dwordx4 v168, s[42:43]
	s_waitcnt vmcnt(16)
	s_waitcnt lgkmcnt(0)
	s_setprio 1
	v_mfma_f32_16x16x128_f8f6f4 v[94:97], v[18:25], v[196:203], 0
	v_mfma_f32_16x16x128_f8f6f4 v[90:93], v[26:33], v[196:203], 0
	v_mfma_f32_16x16x128_f8f6f4 v[82:85], v[18:25], v[204:211], 0
	v_mfma_f32_16x16x128_f8f6f4 v[74:77], v[26:33], v[204:211], 0
	v_mfma_f32_16x16x128_f8f6f4 v[66:69], v[18:25], v[212:219], 0
	v_mfma_f32_16x16x128_f8f6f4 v[58:61], v[26:33], v[212:219], 0
	v_mfma_f32_16x16x128_f8f6f4 v[50:53], v[18:25], v[220:227], 0
	v_mfma_f32_16x16x128_f8f6f4 v[42:45], v[26:33], v[220:227], 0
	s_nop 3
	s_setprio 0
	s_setprio 1
	v_mfma_f32_16x16x128_f8f6f4 v[86:89], v[2:9], v[196:203], 0
	v_mfma_f32_16x16x128_f8f6f4 v[78:81], v[10:17], v[196:203], 0
	v_mfma_f32_16x16x128_f8f6f4 v[70:73], v[2:9], v[204:211], 0
	v_mfma_f32_16x16x128_f8f6f4 v[62:65], v[10:17], v[204:211], 0
	v_mfma_f32_16x16x128_f8f6f4 v[54:57], v[2:9], v[212:219], 0
	v_mfma_f32_16x16x128_f8f6f4 v[46:49], v[10:17], v[212:219], 0
	v_mfma_f32_16x16x128_f8f6f4 v[38:41], v[2:9], v[220:227], 0
	v_mfma_f32_16x16x128_f8f6f4 v[34:37], v[10:17], v[220:227], 0
	s_setprio 0
	s_barrier
; #define PG8_STAGE(bufoff, gbase, voff) do { _Pragma("unroll") for (int _i = 0; _i < 2; ++_i) \
;         __builtin_amdgcn_global_load_lds((const unsigned*)((const char*)(gbase) + (voff)[_i]), (PG8_LAS unsigned*)(lds + (bufoff) + ldsw + _i * 8192), 16, 0, 0); } while (0)
; #define PG8_WAIT_V(n) asm volatile("s_waitcnt vmcnt(" #n ")" ::: "memory")
; #define PG8_WAIT_L(n) asm volatile("s_waitcnt lgkmcnt(" #n ")" ::: "memory")
; #define PG8_BAR __builtin_amdgcn_s_barrier()
; #define PG8_SCHED __builtin_amdgcn_sched_barrier(0)
; template <class Epi, class Sched, bool ALIGN_EPI = true, bool F8 = false>
; __device__ __forceinline__ void gemm_phase(PG8_LAS unsigned char* lds, const Sched& S, const Epi& E) {
;     ...
;             const char* a1 = cA + (size_t)(t + 1) * kstep;
;             const char* a2 = last ? nA : cA + (size_t)(t + 2) * kstep; const char* b2 = last ? nB : cB + (size_t)(t + 2) * kstepB;
;             const char* a3 = a2 + kstep; const char* b3 = b2 + kstepB;
;             unsigned vA2[2][2];
; #pragma unroll
;             for (int h = 0; h < 2; ++h)
; #pragma unroll
;                 for (int i = 0; i < 2; ++i) { if constexpr (Sched::GATHER) vA2[h][i] = (last && has_next) ? voffAn[h][i] : voffA[h][i]; else vA2[h][i] = voffA[h][i]; }
;             PG8_LDB(B0, 0, 0); PG8_LDB(B1, 0, 1); PG8_SCHED; PG8_LDA(At, 0, 0); PG8_STAGE(PG8_SA(1, 1), a1, voffA[1]);
;             PG8_WAIT_V(8); PG8_WAIT_L(0); PG8_BAR; PG8_MMA(0, 0, At, B0); PG8_MMA(0, 1, At, B1); PG8_BAR; PG8_SCHED;
;             PG8_LDA(At, 0, 1); PG8_STAGE(PG8_SB(0, 0), b2, voffB[0]); PG8_STAGE(PG8_SB(0, 1), b2, voffB[1]); PG8_STAGE(PG8_SA(0, 0), a2, vA2[0]);
;             PG8_WAIT_V(8); PG8_WAIT_L(0); PG8_BAR; PG8_MMA(1, 0, At, B0); PG8_MMA(1, 1, At, B1); PG8_BAR; PG8_SCHED;
;             PG8_LDB(B0, 1, 0); PG8_LDB(B1, 1, 1); PG8_SCHED; PG8_LDA(At, 1, 0); PG8_STAGE(PG8_SA(0, 1), a2, vA2[1]);
;             PG8_WAIT_V(8); PG8_WAIT_L(0); PG8_BAR; PG8_MMA(0, 0, At, B0); PG8_MMA(0, 1, At, B1); PG8_BAR; PG8_SCHED;
;             PG8_LDA(At, 1, 1); PG8_STAGE(PG8_SB(1, 0), b3, voffB[0]); PG8_STAGE(PG8_SB(1, 1), b3, voffB[1]); PG8_STAGE(PG8_SA(1, 0), a3, vA2[0]);
;             PG8_WAIT_V(8); PG8_WAIT_L(0); PG8_BAR; PG8_MMA(1, 0, At, B0); PG8_MMA(1, 1, At, B1); PG8_BAR; PG8_SCHED;
	s_add_i32 s66, 0, 0x18000
	s_add_i32 s67, 0, 0x1c000
	v_add_u32_e32 v14, s66, v189
	v_add_u32_e32 v30, s67, v189
	ds_read_b128 v[2:5], v14
	ds_read_b128 v[6:9], v14 offset:1024
	ds_read_b128 v[10:13], v14 offset:2048
	ds_read_b128 v[14:17], v14 offset:3072
	ds_read_b128 v[18:21], v30
	ds_read_b128 v[22:25], v30 offset:1024
	ds_read_b128 v[26:29], v30 offset:2048
	ds_read_b128 v[30:33], v30 offset:3072
	s_mov_b32 m0, s50
	ds_read_b128 v[196:199], v193 offset:32768
	ds_read_b128 v[200:203], v193 offset:33792
	ds_read_b128 v[204:207], v193 offset:34816
	ds_read_b128 v[208:211], v193 offset:35840
	ds_read_b128 v[212:215], v193 offset:36864
	ds_read_b128 v[216:219], v193 offset:37888
	ds_read_b128 v[220:223], v193 offset:38912
	ds_read_b128 v[224:227], v193 offset:39936
	global_load_lds_dwordx4 v172, s[42:43]
	s_mov_b32 m0, s51
	s_nop 0
	global_load_lds_dwordx4 v174, s[42:43]
	s_waitcnt vmcnt(8)
	s_waitcnt lgkmcnt(0)
	s_setprio 1
	v_mfma_f32_16x16x128_f8f6f4 v[158:161], v[2:9], v[196:203], v[158:161]
	v_mfma_f32_16x16x128_f8f6f4 v[154:157], v[10:17], v[196:203], v[154:157]
	v_mfma_f32_16x16x128_f8f6f4 v[150:153], v[2:9], v[204:211], v[150:153]
	v_mfma_f32_16x16x128_f8f6f4 v[146:149], v[10:17], v[204:211], v[146:149]
	v_mfma_f32_16x16x128_f8f6f4 v[130:133], v[2:9], v[212:219], v[130:133]
	v_mfma_f32_16x16x128_f8f6f4 v[122:125], v[10:17], v[212:219], v[122:125]
	v_mfma_f32_16x16x128_f8f6f4 v[114:117], v[2:9], v[220:227], v[114:117]
	v_mfma_f32_16x16x128_f8f6f4 v[106:109], v[10:17], v[220:227], v[106:109]
	s_nop 3
	s_setprio 0
	s_setprio 1
	v_mfma_f32_16x16x128_f8f6f4 v[142:145], v[18:25], v[196:203], v[142:145]
	v_mfma_f32_16x16x128_f8f6f4 v[138:141], v[26:33], v[196:203], v[138:141]
	v_mfma_f32_16x16x128_f8f6f4 v[134:137], v[18:25], v[204:211], v[134:137]
	v_mfma_f32_16x16x128_f8f6f4 v[126:129], v[26:33], v[204:211], v[126:129]
	v_mfma_f32_16x16x128_f8f6f4 v[118:121], v[18:25], v[212:219], v[118:121]
	v_mfma_f32_16x16x128_f8f6f4 v[110:113], v[26:33], v[212:219], v[110:113]
	v_mfma_f32_16x16x128_f8f6f4 v[102:105], v[18:25], v[220:227], v[102:105]
	v_mfma_f32_16x16x128_f8f6f4 v[98:101], v[26:33], v[220:227], v[98:101]
	s_setprio 0
	s_barrier
	s_add_u32 s40, s40, 0x8000
	s_addc_u32 s41, s41, 0
	s_add_i32 s42, s66, s48
	s_mov_b32 m0, s42
	ds_read_b128 v[196:199], v193 offset:49152
	ds_read_b128 v[200:203], v193 offset:50176
	ds_read_b128 v[204:207], v193 offset:51200
	ds_read_b128 v[208:211], v193 offset:52224
	ds_read_b128 v[212:215], v193 offset:53248
	ds_read_b128 v[216:219], v193 offset:54272
	ds_read_b128 v[220:223], v193 offset:55296
	ds_read_b128 v[224:227], v193 offset:56320
	global_load_lds_dwordx4 v162, s[40:41]
	s_add_i32 m0, s42, 0x2000
	s_add_i32 s42, s67, s48
	global_load_lds_dwordx4 v164, s[40:41]
	s_mov_b32 m0, s42
	s_nop 0
	global_load_lds_dwordx4 v176, s[40:41]
	s_add_i32 m0, s42, 0x2000
	s_nop 0
	global_load_lds_dwordx4 v178, s[40:41]
	s_mov_b32 m0, s53
	s_nop 0
	global_load_lds_dwordx4 v166, s[30:31]
	s_mov_b32 m0, s58
	s_nop 0
	global_load_lds_dwordx4 v168, s[30:31]
	s_waitcnt vmcnt(8)
	s_waitcnt lgkmcnt(0)
	s_setprio 1
	v_mfma_f32_16x16x128_f8f6f4 v[94:97], v[2:9], v[196:203], v[94:97]
	v_mfma_f32_16x16x128_f8f6f4 v[90:93], v[10:17], v[196:203], v[90:93]
	v_mfma_f32_16x16x128_f8f6f4 v[82:85], v[2:9], v[204:211], v[82:85]
	v_mfma_f32_16x16x128_f8f6f4 v[74:77], v[10:17], v[204:211], v[74:77]
	v_mfma_f32_16x16x128_f8f6f4 v[66:69], v[2:9], v[212:219], v[66:69]
	v_mfma_f32_16x16x128_f8f6f4 v[58:61], v[10:17], v[212:219], v[58:61]
	v_mfma_f32_16x16x128_f8f6f4 v[50:53], v[2:9], v[220:227], v[50:53]
	v_mfma_f32_16x16x128_f8f6f4 v[42:45], v[10:17], v[220:227], v[42:45]
	s_nop 3
	s_setprio 0
	s_setprio 1
	v_mfma_f32_16x16x128_f8f6f4 v[86:89], v[18:25], v[196:203], v[86:89]
	v_mfma_f32_16x16x128_f8f6f4 v[78:81], v[26:33], v[196:203], v[78:81]
	v_mfma_f32_16x16x128_f8f6f4 v[70:73], v[18:25], v[204:211], v[70:73]
	v_mfma_f32_16x16x128_f8f6f4 v[62:65], v[26:33], v[204:211], v[62:65]
	v_mfma_f32_16x16x128_f8f6f4 v[54:57], v[18:25], v[212:219], v[54:57]
	v_mfma_f32_16x16x128_f8f6f4 v[46:49], v[26:33], v[212:219], v[46:49]
	v_mfma_f32_16x16x128_f8f6f4 v[38:41], v[18:25], v[220:227], v[38:41]
	v_mfma_f32_16x16x128_f8f6f4 v[34:37], v[26:33], v[220:227], v[34:37]
	s_setprio 0
	s_barrier
	s_add_i32 s65, s65, 2
	s_add_u32 s19, s19, 0x10000
	s_addc_u32 s21, s21, 0
	s_add_u32 s28, s28, 0x10000
	s_addc_u32 s29, s29, 0
	s_cmp_gt_u32 s65, 13
	s_cbranch_scc0 .LBB0_911
	s_branch .Lfx_26630

; #define PG8_STAGE(bufoff, gbase, voff) do { _Pragma("unroll") for (int _i = 0; _i < 2; ++_i) \
;         __builtin_amdgcn_global_load_lds((const unsigned*)((const char*)(gbase) + (voff)[_i]), (PG8_LAS unsigned*)(lds + (bufoff) + ldsw + _i * 8192), 16, 0, 0); } while (0)
; template <class Epi, class Sched, bool ALIGN_EPI = true, bool F8 = false>
; __device__ __forceinline__ void gemm_phase(PG8_LAS unsigned char* lds, const Sched& S, const Epi& E) {
;     ...
;         const bool has_next = S.next(ui + 1, nxt);
;         const char* nA = has_next ? nxt.A : cA; const char* nB = has_next ? nxt.B : cB;
;         const int nt = cur.nt;
; #pragma unroll 1
;         for (int t = 0; t < nt; t += 2) {
;             const bool last = (t == nt - 2);
;             if constexpr (Sched::GATHER) { if (last && has_next) S.a_off(nxt, Rs, Cs, voffAn); }
;             const char* a1 = cA + (size_t)(t + 1) * kstep;
;             const char* a2 = last ? nA : cA + (size_t)(t + 2) * kstep; const char* b2 = last ? nB : cB + (size_t)(t + 2) * kstepB;
;             const char* a3 = a2 + kstep; const char* b3 = b2 + kstepB;
;             unsigned vA2[2][2];
; #pragma unroll
;             for (int h = 0; h < 2; ++h)
; #pragma unroll
;                 for (int i = 0; i < 2; ++i) { if constexpr (Sched::GATHER) vA2[h][i] = (last && has_next) ? voffAn[h][i] : voffA[h][i]; else vA2[h][i] = voffA[h][i]; }
;             PG8_LDB(B0, 0, 0); PG8_LDB(B1, 0, 1); PG8_SCHED; PG8_LDA(At, 0, 0); PG8_STAGE(PG8_SA(1, 1), a1, voffA[1]);
;             PG8_WAIT_V(8); PG8_WAIT_L(0); PG8_BAR; PG8_MMA(0, 0, At, B0); PG8_MMA(0, 1, At, B1); PG8_BAR; PG8_SCHED;
;             PG8_LDA(At, 0, 1); PG8_STAGE(PG8_SB(0, 0), b2, voffB[0]); PG8_STAGE(PG8_SB(0, 1), b2, voffB[1]); PG8_STAGE(PG8_SA(0, 0), a2, vA2[0]);
;             PG8_WAIT_V(8); PG8_WAIT_L(0); PG8_BAR; PG8_MMA(1, 0, At, B0); PG8_MMA(1, 1, At, B1); PG8_BAR; PG8_SCHED;
;             PG8_LDB(B0, 1, 0); PG8_LDB(B1, 1, 1); PG8_SCHED; PG8_LDA(At, 1, 0); PG8_STAGE(PG8_SA(0, 1), a2, vA2[1]);
;             PG8_WAIT_V(8); PG8_WAIT_L(0); PG8_BAR; PG8_MMA(0, 0, At, B0); PG8_MMA(0, 1, At, B1); PG8_BAR; PG8_SCHED;
;             PG8_LDA(At, 1, 1); PG8_STAGE(PG8_SB(1, 0), b3, voffB[0]); PG8_STAGE(PG8_SB(1, 1), b3, voffB[1]); PG8_STAGE(PG8_SA(1, 0), a3, vA2[0]);
;             PG8_WAIT_V(8); PG8_WAIT_L(0); PG8_BAR; PG8_MMA(1, 0, At, B0); PG8_MMA(1, 1, At, B1); PG8_BAR; PG8_SCHED;
.Lh1e_26630:
.Lpk1_911:
	ds_read_b128 v[18:21], v191
	ds_read_b128 v[22:25], v191 offset:1024
	ds_read_b128 v[26:29], v191 offset:2048
	ds_read_b128 v[30:33], v191 offset:3072
	ds_read_b128 v[2:5], v192
	ds_read_b128 v[6:9], v192 offset:1024
	ds_read_b128 v[10:13], v192 offset:2048
	ds_read_b128 v[14:17], v192 offset:3072
	s_add_u32 s30, s28, 0x8000
	s_addc_u32 s31, s29, 0
	s_cmp_eq_u32 s65, 12
	s_cselect_b32 s42, s22, s30
	s_cselect_b32 s43, s23, s31
	s_cselect_b32 s40, s24, s19
	s_cselect_b32 s41, s25, s21
	s_add_u32 s30, s42, 0x8000
	s_addc_u32 s31, s43, 0
	s_add_i32 m0, s27, 0xc000
	ds_read_b128 v[196:199], v193
	ds_read_b128 v[200:203], v193 offset:1024
	ds_read_b128 v[204:207], v193 offset:2048
	ds_read_b128 v[208:211], v193 offset:3072
	ds_read_b128 v[212:215], v193 offset:4096
	ds_read_b128 v[216:219], v193 offset:5120
	ds_read_b128 v[220:223], v193 offset:6144
	ds_read_b128 v[224:227], v193 offset:7168
	global_load_lds_dwordx4 v182, s[28:29]
	s_add_i32 m0, s27, 0xe000
	s_nop 0
	global_load_lds_dwordx4 v180, s[28:29]
	s_waitcnt vmcnt(16)
	s_waitcnt lgkmcnt(0)
	s_barrier
	s_setprio 2
	v_mfma_f32_16x16x128_f8f6f4 v[158:161], v[18:25], v[196:203], 0
	v_mfma_f32_16x16x128_f8f6f4 v[154:157], v[26:33], v[196:203], 0
	v_mfma_f32_16x16x128_f8f6f4 v[150:153], v[18:25], v[204:211], 0
	v_mfma_f32_16x16x128_f8f6f4 v[146:149], v[26:33], v[204:211], 0
	v_mfma_f32_16x16x128_f8f6f4 v[130:133], v[18:25], v[212:219], 0
	v_mfma_f32_16x16x128_f8f6f4 v[122:125], v[26:33], v[212:219], 0
	v_mfma_f32_16x16x128_f8f6f4 v[114:117], v[18:25], v[220:227], 0
	v_mfma_f32_16x16x128_f8f6f4 v[106:109], v[26:33], v[220:227], 0
	s_nop 3
	s_setprio 0
	s_setprio 2
	v_mfma_f32_16x16x128_f8f6f4 v[142:145], v[2:9], v[196:203], 0
	v_mfma_f32_16x16x128_f8f6f4 v[138:141], v[10:17], v[196:203], 0
	v_mfma_f32_16x16x128_f8f6f4 v[134:137], v[2:9], v[204:211], 0
	v_mfma_f32_16x16x128_f8f6f4 v[126:129], v[10:17], v[204:211], 0
	v_mfma_f32_16x16x128_f8f6f4 v[118:121], v[2:9], v[212:219], 0
	v_mfma_f32_16x16x128_f8f6f4 v[110:113], v[10:17], v[212:219], 0
	v_mfma_f32_16x16x128_f8f6f4 v[102:105], v[2:9], v[220:227], 0
	v_mfma_f32_16x16x128_f8f6f4 v[98:101], v[10:17], v[220:227], 0
	s_setprio 0
	s_add_i32 s66, s60, s48
	s_mov_b32 m0, s66
	ds_read_b128 v[196:199], v193 offset:16384
	ds_read_b128 v[200:203], v193 offset:17408
	ds_read_b128 v[204:207], v193 offset:18432
	ds_read_b128 v[208:211], v193 offset:19456
	ds_read_b128 v[212:215], v193 offset:20480
	ds_read_b128 v[216:219], v193 offset:21504
	ds_read_b128 v[220:223], v193 offset:22528
	ds_read_b128 v[224:227], v193 offset:23552
	global_load_lds_dwordx4 v162, s[40:41]
	s_add_i32 m0, s66, 0x2000
	s_add_i32 s66, s61, s48
	global_load_lds_dwordx4 v164, s[40:41]
	s_add_u32 s98, s40, s6
	s_addc_u32 s99, s41, s7
	s_mov_b32 m0, s66
	s_nop 0
	global_load_lds_dwordx4 v162, s[98:99]
	s_add_u32 s100, s40, s6
	s_addc_u32 s101, s41, s7
	s_add_i32 m0, s66, 0x2000
	s_nop 0
	global_load_lds_dwordx4 v164, s[100:101]
	s_mov_b32 m0, s27
	s_nop 0
	global_load_lds_dwordx4 v166, s[42:43]
	s_mov_b32 m0, s49
	s_nop 0
	global_load_lds_dwordx4 v168, s[42:43]
	s_waitcnt vmcnt(16)
	s_waitcnt lgkmcnt(0)
	s_barrier
	s_setprio 2
	v_mfma_f32_16x16x128_f8f6f4 v[94:97], v[18:25], v[196:203], 0
	v_mfma_f32_16x16x128_f8f6f4 v[90:93], v[26:33], v[196:203], 0
	v_mfma_f32_16x16x128_f8f6f4 v[82:85], v[18:25], v[204:211], 0
	v_mfma_f32_16x16x128_f8f6f4 v[74:77], v[26:33], v[204:211], 0
	v_mfma_f32_16x16x128_f8f6f4 v[66:69], v[18:25], v[212:219], 0
	v_mfma_f32_16x16x128_f8f6f4 v[58:61], v[26:33], v[212:219], 0
	v_mfma_f32_16x16x128_f8f6f4 v[50:53], v[18:25], v[220:227], 0
	v_mfma_f32_16x16x128_f8f6f4 v[42:45], v[26:33], v[220:227], 0
	s_nop 3
	s_setprio 0
	s_setprio 2
	v_mfma_f32_16x16x128_f8f6f4 v[86:89], v[2:9], v[196:203], 0
	v_mfma_f32_16x16x128_f8f6f4 v[78:81], v[10:17], v[196:203], 0
	v_mfma_f32_16x16x128_f8f6f4 v[70:73], v[2:9], v[204:211], 0
	v_mfma_f32_16x16x128_f8f6f4 v[62:65], v[10:17], v[204:211], 0
	v_mfma_f32_16x16x128_f8f6f4 v[54:57], v[2:9], v[212:219], 0
	v_mfma_f32_16x16x128_f8f6f4 v[46:49], v[10:17], v[212:219], 0
	v_mfma_f32_16x16x128_f8f6f4 v[38:41], v[2:9], v[220:227], 0
	v_mfma_f32_16x16x128_f8f6f4 v[34:37], v[10:17], v[220:227], 0
	s_setprio 0
	s_add_i32 s66, 0, 0x18000
	s_add_i32 s67, 0, 0x1c000
	v_add_u32_e32 v14, s66, v189
	v_add_u32_e32 v30, s67, v189
	ds_read_b128 v[2:5], v14
	ds_read_b128 v[6:9], v14 offset:1024
	ds_read_b128 v[10:13], v14 offset:2048
	ds_read_b128 v[14:17], v14 offset:3072
	ds_read_b128 v[18:21], v30
	ds_read_b128 v[22:25], v30 offset:1024
	ds_read_b128 v[26:29], v30 offset:2048
	ds_read_b128 v[30:33], v30 offset:3072
	s_mov_b32 m0, s50
	ds_read_b128 v[196:199], v193 offset:32768
	ds_read_b128 v[200:203], v193 offset:33792
	ds_read_b128 v[204:207], v193 offset:34816
	ds_read_b128 v[208:211], v193 offset:35840
	ds_read_b128 v[212:215], v193 offset:36864
	ds_read_b128 v[216:219], v193 offset:37888
	ds_read_b128 v[220:223], v193 offset:38912
	ds_read_b128 v[224:227], v193 offset:39936
	global_load_lds_dwordx4 v172, s[42:43]
	s_mov_b32 m0, s51
	s_nop 0
	global_load_lds_dwordx4 v174, s[42:43]
	s_waitcnt vmcnt(8)
	s_waitcnt lgkmcnt(0)
	s_barrier
; #define PG8_STAGE(bufoff, gbase, voff) do { _Pragma("unroll") for (int _i = 0; _i < 2; ++_i) \
;         __builtin_amdgcn_global_load_lds((const unsigned*)((const char*)(gbase) + (voff)[_i]), (PG8_LAS unsigned*)(lds + (bufoff) + ldsw + _i * 8192), 16, 0, 0); } while (0)
; #define PG8_WAIT_V(n) asm volatile("s_waitcnt vmcnt(" #n ")" ::: "memory")
; #define PG8_WAIT_L(n) asm volatile("s_waitcnt lgkmcnt(" #n ")" ::: "memory")
; #define PG8_BAR __builtin_amdgcn_s_barrier()
; #define PG8_SCHED __builtin_amdgcn_sched_barrier(0)
; template <class Epi, class Sched, bool ALIGN_EPI = true, bool F8 = false>
; __device__ __forceinline__ void gemm_phase(PG8_LAS unsigned char* lds, const Sched& S, const Epi& E) {
;     ...
;             const char* a1 = cA + (size_t)(t + 1) * kstep;
;             const char* a2 = last ? nA : cA + (size_t)(t + 2) * kstep; const char* b2 = last ? nB : cB + (size_t)(t + 2) * kstepB;
;             const char* a3 = a2 + kstep; const char* b3 = b2 + kstepB;
;             unsigned vA2[2][2];
; #pragma unroll
;             for (int h = 0; h < 2; ++h)
; #pragma unroll
;                 for (int i = 0; i < 2; ++i) { if constexpr (Sched::GATHER) vA2[h][i] = (last && has_next) ? voffAn[h][i] : voffA[h][i]; else vA2[h][i] = voffA[h][i]; }
;             PG8_LDB(B0, 0, 0); PG8_LDB(B1, 0, 1); PG8_SCHED; PG8_LDA(At, 0, 0); PG8_STAGE(PG8_SA(1, 1), a1, voffA[1]);
;             PG8_WAIT_V(8); PG8_WAIT_L(0); PG8_BAR; PG8_MMA(0, 0, At, B0); PG8_MMA(0, 1, At, B1); PG8_BAR; PG8_SCHED;
;             PG8_LDA(At, 0, 1); PG8_STAGE(PG8_SB(0, 0), b2, voffB[0]); PG8_STAGE(PG8_SB(0, 1), b2, voffB[1]); PG8_STAGE(PG8_SA(0, 0), a2, vA2[0]);
;             PG8_WAIT_V(8); PG8_WAIT_L(0); PG8_BAR; PG8_MMA(1, 0, At, B0); PG8_MMA(1, 1, At, B1); PG8_BAR; PG8_SCHED;
;             PG8_LDB(B0, 1, 0); PG8_LDB(B1, 1, 1); PG8_SCHED; PG8_LDA(At, 1, 0); PG8_STAGE(PG8_SA(0, 1), a2, vA2[1]);
;             PG8_WAIT_V(8); PG8_WAIT_L(0); PG8_BAR; PG8_MMA(0, 0, At, B0); PG8_MMA(0, 1, At, B1); PG8_BAR; PG8_SCHED;
;             PG8_LDA(At, 1, 1); PG8_STAGE(PG8_SB(1, 0), b3, voffB[0]); PG8_STAGE(PG8_SB(1, 1), b3, voffB[1]); PG8_STAGE(PG8_SA(1, 0), a3, vA2[0]);
;             PG8_WAIT_V(8); PG8_WAIT_L(0); PG8_BAR; PG8_MMA(1, 0, At, B0); PG8_MMA(1, 1, At, B1); PG8_BAR; PG8_SCHED;
	s_setprio 2
	v_mfma_f32_16x16x128_f8f6f4 v[158:161], v[2:9], v[196:203], v[158:161]
	v_mfma_f32_16x16x128_f8f6f4 v[154:157], v[10:17], v[196:203], v[154:157]
	v_mfma_f32_16x16x128_f8f6f4 v[150:153], v[2:9], v[204:211], v[150:153]
	v_mfma_f32_16x16x128_f8f6f4 v[146:149], v[10:17], v[204:211], v[146:149]
	v_mfma_f32_16x16x128_f8f6f4 v[130:133], v[2:9], v[212:219], v[130:133]
	v_mfma_f32_16x16x128_f8f6f4 v[122:125], v[10:17], v[212:219], v[122:125]
	v_mfma_f32_16x16x128_f8f6f4 v[114:117], v[2:9], v[220:227], v[114:117]
	v_mfma_f32_16x16x128_f8f6f4 v[106:109], v[10:17], v[220:227], v[106:109]
	s_nop 3
	s_setprio 0
	s_setprio 2
	v_mfma_f32_16x16x128_f8f6f4 v[142:145], v[18:25], v[196:203], v[142:145]
	v_mfma_f32_16x16x128_f8f6f4 v[138:141], v[26:33], v[196:203], v[138:141]
	v_mfma_f32_16x16x128_f8f6f4 v[134:137], v[18:25], v[204:211], v[134:137]
	v_mfma_f32_16x16x128_f8f6f4 v[126:129], v[26:33], v[204:211], v[126:129]
	v_mfma_f32_16x16x128_f8f6f4 v[118:121], v[18:25], v[212:219], v[118:121]
	v_mfma_f32_16x16x128_f8f6f4 v[110:113], v[26:33], v[212:219], v[110:113]
	v_mfma_f32_16x16x128_f8f6f4 v[102:105], v[18:25], v[220:227], v[102:105]
	v_mfma_f32_16x16x128_f8f6f4 v[98:101], v[26:33], v[220:227], v[98:101]
	s_setprio 0
	s_add_u32 s40, s40, 0x8000
	s_addc_u32 s41, s41, 0
	s_add_i32 s42, s66, s48
	s_mov_b32 m0, s42
	ds_read_b128 v[196:199], v193 offset:49152
	ds_read_b128 v[200:203], v193 offset:50176
	ds_read_b128 v[204:207], v193 offset:51200
	ds_read_b128 v[208:211], v193 offset:52224
	ds_read_b128 v[212:215], v193 offset:53248
	ds_read_b128 v[216:219], v193 offset:54272
	ds_read_b128 v[220:223], v193 offset:55296
	ds_read_b128 v[224:227], v193 offset:56320
	global_load_lds_dwordx4 v162, s[40:41]
	s_add_i32 m0, s42, 0x2000
	s_add_i32 s42, s67, s48
	global_load_lds_dwordx4 v164, s[40:41]
	s_mov_b32 m0, s42
	s_nop 0
	global_load_lds_dwordx4 v176, s[40:41]
	s_add_i32 m0, s42, 0x2000
	s_nop 0
	global_load_lds_dwordx4 v178, s[40:41]
	s_mov_b32 m0, s53
	s_nop 0
	global_load_lds_dwordx4 v166, s[30:31]
	s_mov_b32 m0, s58
	s_nop 0
	global_load_lds_dwordx4 v168, s[30:31]
	s_waitcnt vmcnt(8)
	s_waitcnt lgkmcnt(0)
	s_barrier
	s_setprio 2
	v_mfma_f32_16x16x128_f8f6f4 v[94:97], v[2:9], v[196:203], v[94:97]
	v_mfma_f32_16x16x128_f8f6f4 v[90:93], v[10:17], v[196:203], v[90:93]
	v_mfma_f32_16x16x128_f8f6f4 v[82:85], v[2:9], v[204:211], v[82:85]
	v_mfma_f32_16x16x128_f8f6f4 v[74:77], v[10:17], v[204:211], v[74:77]
	v_mfma_f32_16x16x128_f8f6f4 v[66:69], v[2:9], v[212:219], v[66:69]
	v_mfma_f32_16x16x128_f8f6f4 v[58:61], v[10:17], v[212:219], v[58:61]
	v_mfma_f32_16x16x128_f8f6f4 v[50:53], v[2:9], v[220:227], v[50:53]
	v_mfma_f32_16x16x128_f8f6f4 v[42:45], v[10:17], v[220:227], v[42:45]
	s_nop 3
	s_setprio 0
	s_setprio 2
	v_mfma_f32_16x16x128_f8f6f4 v[86:89], v[18:25], v[196:203], v[86:89]
	v_mfma_f32_16x16x128_f8f6f4 v[78:81], v[26:33], v[196:203], v[78:81]
	v_mfma_f32_16x16x128_f8f6f4 v[70:73], v[18:25], v[204:211], v[70:73]
	v_mfma_f32_16x16x128_f8f6f4 v[62:65], v[26:33], v[204:211], v[62:65]
	v_mfma_f32_16x16x128_f8f6f4 v[54:57], v[18:25], v[212:219], v[54:57]
	v_mfma_f32_16x16x128_f8f6f4 v[46:49], v[26:33], v[212:219], v[46:49]
	v_mfma_f32_16x16x128_f8f6f4 v[38:41], v[18:25], v[220:227], v[38:41]
	v_mfma_f32_16x16x128_f8f6f4 v[34:37], v[26:33], v[220:227], v[34:37]
	s_setprio 0
	s_add_i32 s65, s65, 2
	s_add_u32 s19, s19, 0x10000
	s_addc_u32 s21, s21, 0
	s_add_u32 s28, s28, 0x10000
	s_addc_u32 s29, s29, 0
	s_cmp_gt_u32 s65, 13
	s_cbranch_scc0 .Lh1_911
	s_branch .Lfx_26630
